# attention<16> (layer 3) tile loop unrolled by LDS buffer parity like layers 0-2
# baseline (speedup 1.0000x reference)
.LBB0_1276:
	v_readlane_b32 s0, v251, 54
	v_readlane_b32 s1, v251, 55
	s_andn2_b64 vcc, exec, s[0:1]
	v_readfirstlane_b32 s0, v219
	s_waitcnt lgkmcnt(0)
	s_barrier
	s_cbranch_vccnz .LBB0_1292
	v_lshrrev_b32_e32 v0, 2, v219
	v_and_or_b32 v0, v0, 4, v167
	s_ashr_i32 s6, s0, 6
	v_lshlrev_b32_e32 v3, 1, v0
	v_or_b32_e32 v0, v170, v167
	s_lshl_b32 s7, s6, 3
	v_lshlrev_b32_e32 v0, 8, v0
	s_waitcnt vmcnt(14)
	v_and_b32_e32 v4, 8, v220
	v_lshrrev_b32_e32 v1, 4, v219
	v_add3_u32 v220, 0, v0, v4
	v_bitop3_b32 v0, s7, v219, v159 bitop3:0x36
	v_mov_b32_e32 v171, v33
	v_lshlrev_b32_e32 v0, 3, v0
	v_bitop3_b32 v1, v1, v166, 3 bitop3:0x6c
	s_and_b32 s10, s0, 0xffffff80
	s_lshl_b32 s0, s6, 5
	v_or_b32_e32 v2, s7, v159
	v_lshl_add_u64 v[172:173], s[4:5], 0, v[170:171]
	v_and_b32_e32 v176, 0x78, v0
	v_lshlrev_b32_e32 v0, 3, v166
	v_lshlrev_b32_e32 v4, 4, v159
	v_lshlrev_b32_e32 v171, 4, v1
	v_bitop3_b32 v1, v159, v166, 4 bitop3:0x36
	v_and_or_b32 v177, s0, 32, v166
	v_bfe_u32 v5, v219, 1, 1
	v_mad_i64_i32 v[174:175], s[0:1], v2, s96, 0
	v_xor_b32_e32 v0, v4, v0
	v_or_b32_e32 v4, 4, v2
	v_bitop3_b32 v2, v2, v219, 4 bitop3:0x36
	v_lshlrev_b32_e32 v219, 4, v1
	v_bitop3_b32 v1, v159, v166, 8 bitop3:0x36
	v_lshlrev_b32_e32 v222, 4, v1
	v_bitop3_b32 v1, v159, v166, 12 bitop3:0x36
	v_lshlrev_b32_e32 v223, 4, v1
	v_or_b32_e32 v1, v3, v5
	v_lshlrev_b32_e32 v224, 4, v1
	v_bitop3_b32 v1, v3, v5, 2 bitop3:0x1e
	v_lshlrev_b32_e32 v225, 4, v1
	v_bitop3_b32 v1, v3, v5, 4 bitop3:0x1e
	v_mad_i64_i32 v[178:179], s[0:1], v4, s96, 0
	v_lshlrev_b32_e32 v237, 4, v1
	v_bitop3_b32 v1, v3, v5, 6 bitop3:0x1e
	v_lshlrev_b32_e32 v238, 4, v1
	v_bitop3_b32 v1, v3, v5, 8 bitop3:0x1e
	s_lshl_b32 s0, s6, 14
	v_lshlrev_b32_e32 v4, 1, v4
	v_lshlrev_b32_e32 v239, 4, v1
	v_bitop3_b32 v1, v3, v5, 10 bitop3:0x1e
	s_and_b32 s0, s0, 0x4000
	v_lshlrev_b32_e32 v2, 3, v2
	v_bitop3_b32 v4, v4, v166, 14 bitop3:0x6c
	v_lshlrev_b32_e32 v240, 4, v1
	v_bitop3_b32 v1, v3, v5, 12 bitop3:0x1e
	s_add_i32 s0, s0, 0
	s_lshl_b32 s8, s6, 11
	v_and_b32_e32 v2, 0x78, v2
	v_lshlrev_b32_e32 v4, 3, v4
	v_add_u32_e32 v180, 0x2000, v168
	v_add_u32_e32 v182, 0x4000, v168
	v_add_u32_e32 v184, 0x6000, v168
	v_lshlrev_b32_e32 v241, 4, v1
	v_bitop3_b32 v1, v3, v5, 14 bitop3:0x1e
	s_add_i32 s0, s0, 0x10000
	s_addk_i32 s7, 0x44
	v_lshl_add_u32 v221, v166, 8, 0
	s_add_i32 s11, s8, 0
	v_ashrrev_i32_e32 v169, 31, v168
	v_ashrrev_i32_e32 v181, 31, v180
	v_ashrrev_i32_e32 v183, 31, v182
	v_ashrrev_i32_e32 v185, 31, v184
	v_lshlrev_b32_e32 v242, 4, v1
	v_lshl_add_u32 v243, v166, 9, s0
	v_or_b32_e32 v244, s7, v159
	v_lshlrev_b32_e32 v166, 1, v0
	v_lshlrev_b32_e32 v186, 1, v2
	v_lshlrev_b32_e32 v188, 1, v4
	v_add3_u32 v166, v174, v166, s90
	v_add3_u32 v186, v178, v186, s84
	v_add3_u32 v188, v178, v188, s90
	v_lshlrev_b32_e32 v190, 1, v158
	v_add_u32_e32 v171, v221, v171
	v_add_u32_e32 v219, v221, v219
	v_add_u32_e32 v222, v221, v222
	v_add_u32_e32 v223, v221, v223
	v_add_u32_e32 v224, v220, v224
	v_add_u32_e32 v225, v220, v225
	v_add_u32_e32 v237, v220, v237
	v_add_u32_e32 v238, v220, v238
	v_add_u32_e32 v239, v220, v239
	v_add_u32_e32 v240, v220, v240
	v_add_u32_e32 v241, v220, v241
	v_add_u32_e32 v242, v220, v242
	s_mov_b32 s12, s83
	s_branch .LBB0_1279

.LBB0_1284:
	s_mov_b64 s[8:9], 0
.LBB0_1285:
	s_andn2_b64 vcc, exec, s[8:9]
	s_cbranch_vccnz .LBB0_1287
	s_add_i32 s20, s11, 0x4000
	s_mov_b32 m0, s20
	s_nop 0
	global_load_lds_dwordx4 v32, s[100:101]
	s_add_i32 m0, s20, 0x8000
	s_nop 0
	global_load_lds_dwordx4 v166, s[100:101]
	s_add_i32 m0, s20, 0x400
	s_nop 0
	global_load_lds_dwordx4 v186, s[100:101]
	s_add_i32 m0, s20, 0x8400
	s_nop 0
	global_load_lds_dwordx4 v188, s[100:101]
	s_add_u32 s100, s100, 0x240000
	s_addc_u32 s101, s101, 0
.LBB0_1287:
	ds_read_b128 v[102:105], v171
	ds_read_b128 v[106:109], v219
	ds_read_b128 v[110:113], v222
	ds_read_b128 v[114:117], v223
	ds_read_b128 v[118:121], v171 offset:4096
	ds_read_b128 v[122:125], v219 offset:4096
	ds_read_b128 v[126:129], v222 offset:4096
	ds_read_b128 v[130:133], v223 offset:4096
	s_waitcnt lgkmcnt(0)
	v_mfma_f32_16x16x32_bf16 v[138:141], v[118:121], v[78:81], 0
	v_mfma_f32_16x16x32_bf16 v[134:137], v[102:105], v[78:81], 0
	v_mfma_f32_16x16x32_bf16 v[102:105], v[102:105], v[94:97], 0
	v_mfma_f32_16x16x32_bf16 v[118:121], v[118:121], v[94:97], 0
	v_mfma_f32_16x16x32_bf16 v[134:137], v[106:109], v[70:73], v[134:137]
	v_mfma_f32_16x16x32_bf16 v[102:105], v[106:109], v[86:89], v[102:105]
	v_mfma_f32_16x16x32_bf16 v[138:141], v[122:125], v[70:73], v[138:141]
	v_mfma_f32_16x16x32_bf16 v[118:121], v[122:125], v[86:89], v[118:121]
	v_mfma_f32_16x16x32_bf16 v[134:137], v[110:113], v[74:77], v[134:137]
	v_mfma_f32_16x16x32_bf16 v[102:105], v[110:113], v[90:93], v[102:105]
	v_mfma_f32_16x16x32_bf16 v[138:141], v[126:129], v[74:77], v[138:141]
	v_mfma_f32_16x16x32_bf16 v[118:121], v[126:129], v[90:93], v[118:121]
	v_mfma_f32_16x16x32_bf16 v[162:165], v[114:117], v[82:85], v[134:137]
	v_mfma_f32_16x16x32_bf16 v[134:137], v[114:117], v[98:101], v[102:105]
	s_nop 3
	ds_read_b128 v[102:105], v171 offset:8192
	ds_read_b128 v[106:109], v219 offset:8192
	ds_read_b128 v[110:113], v222 offset:8192
	ds_read_b128 v[114:117], v223 offset:8192
	v_max_f32_e32 v167, v164, v165
	v_mfma_f32_16x16x32_bf16 v[158:161], v[130:133], v[82:85], v[138:141]
	v_max3_f32 v167, v162, v163, v167
	v_mfma_f32_16x16x32_bf16 v[138:141], v[130:133], v[98:101], v[118:121]
	s_nop 2
	ds_read_b128 v[118:121], v171 offset:12288
	ds_read_b128 v[122:125], v219 offset:12288
	ds_read_b128 v[126:129], v222 offset:12288
	ds_read_b128 v[130:133], v223 offset:12288
	v_max3_f32 v189, v159, v160, v161
	v_max3_f32 v167, v167, v158, v189
	s_waitcnt lgkmcnt(0)
	v_mfma_f32_16x16x32_bf16 v[142:145], v[102:105], v[78:81], 0
	v_mfma_f32_16x16x32_bf16 v[102:105], v[102:105], v[94:97], 0
	v_mfma_f32_16x16x32_bf16 v[102:105], v[106:109], v[86:89], v[102:105]
	v_mfma_f32_16x16x32_bf16 v[102:105], v[110:113], v[90:93], v[102:105]
	v_mfma_f32_16x16x32_bf16 v[146:149], v[114:117], v[98:101], v[102:105]
	v_mfma_f32_16x16x32_bf16 v[102:105], v[118:121], v[78:81], 0
	v_mfma_f32_16x16x32_bf16 v[142:145], v[106:109], v[70:73], v[142:145]
	v_mfma_f32_16x16x32_bf16 v[102:105], v[122:125], v[70:73], v[102:105]
	v_mfma_f32_16x16x32_bf16 v[142:145], v[110:113], v[74:77], v[142:145]
	v_mfma_f32_16x16x32_bf16 v[102:105], v[126:129], v[74:77], v[102:105]
	v_mfma_f32_16x16x32_bf16 v[154:157], v[114:117], v[82:85], v[142:145]
	v_mfma_f32_16x16x32_bf16 v[150:153], v[130:133], v[82:85], v[102:105]
	v_mfma_f32_16x16x32_bf16 v[102:105], v[118:121], v[94:97], 0
	s_nop 5
	v_max3_f32 v189, v155, v156, v157
	v_max3_f32 v167, v167, v154, v189
	v_max3_f32 v189, v151, v152, v153
	v_mfma_f32_16x16x32_bf16 v[102:105], v[122:125], v[86:89], v[102:105]
	v_max3_f32 v167, v167, v150, v189
	v_mov_b32_e32 v189, v167
	s_nop 1
	v_permlane16_swap_b32_e32 v167, v189
	v_mfma_f32_16x16x32_bf16 v[102:105], v[126:129], v[90:93], v[102:105]
	v_max_f32 v167, v167, v189
	s_nop 0
	v_mov_b32_e32 v189, v167
	s_nop 1
	v_permlane32_swap_b32_e32 v167, v189
	v_max_f32 v167, v167, v189
	v_mfma_f32_16x16x32_bf16 v[142:145], v[130:133], v[98:101], v[102:105]
	v_mul_f32_e32 v167, 0x3e0293ee, v167
	v_add_f32_e32 v189, 0x41000000, v246
	v_cmp_gt_f32_e32 vcc, v167, v189
	ds_read_b64_tr_b16 v[130:131], v224 offset:32768
	ds_read_b64_tr_b16 v[132:133], v224 offset:36864
	ds_read_b64_tr_b16 v[122:123], v224 offset:40960
	ds_read_b64_tr_b16 v[124:125], v224 offset:45056
	ds_read_b64_tr_b16 v[126:127], v225 offset:32768
	ds_read_b64_tr_b16 v[128:129], v225 offset:36864
	ds_read_b64_tr_b16 v[114:115], v225 offset:40960
	ds_read_b64_tr_b16 v[116:117], v225 offset:45056
	v_cndmask_b32_e32 v189, v246, v167, vcc
	ds_read_b64_tr_b16 v[118:119], v237 offset:32768
	ds_read_b64_tr_b16 v[120:121], v237 offset:36864
	ds_read_b64_tr_b16 v[110:111], v237 offset:40960
	ds_read_b64_tr_b16 v[112:113], v237 offset:45056
	ds_read_b64_tr_b16 v[106:107], v238 offset:32768
	ds_read_b64_tr_b16 v[108:109], v238 offset:36864
	ds_read_b64_tr_b16 v[102:103], v238 offset:40960
	ds_read_b64_tr_b16 v[104:105], v238 offset:45056
	ds_read_b64 v[198:199], v213
	v_fma_f32 v162, v162, s97, -v189
	v_exp_f32_e32 v162, v162
	v_fma_f32 v163, v163, s97, -v189
	v_exp_f32_e32 v163, v163
	v_fma_f32 v164, v164, s97, -v189
	v_exp_f32_e32 v164, v164
	v_fma_f32 v165, v165, s97, -v189
	v_exp_f32_e32 v165, v165
	v_fma_f32 v158, v158, s97, -v189
	s_waitcnt lgkmcnt(0)
	v_lshrrev_b64 v[216:217], v170, v[198:199]
	v_bfe_i32 v198, v216, 0, 1
	v_exp_f32_e32 v158, v158
	v_and_b32_e32 v162, v198, v162
	v_fma_f32 v159, v159, s97, -v189
	v_bfe_i32 v199, v216, 1, 1
	v_and_b32_e32 v163, v199, v163
	v_exp_f32_e32 v159, v159
	v_fma_f32 v160, v160, s97, -v189
	v_add_f32_e32 v198, v162, v163
	v_bfe_i32 v199, v216, 2, 1
	v_exp_f32_e32 v160, v160
	v_and_b32_e32 v164, v199, v164
	v_fma_f32 v161, v161, s97, -v189
	v_bfe_i32 v200, v216, 3, 1
	v_add_f32_e32 v198, v198, v164
	v_and_b32_e32 v165, v200, v165
	v_exp_f32_e32 v161, v161
	v_fma_f32 v154, v154, s97, -v189
	v_add_f32_e32 v198, v198, v165
	v_bfe_i32 v199, v216, 16, 1
	v_exp_f32_e32 v154, v154
	v_and_b32_e32 v158, v199, v158
	v_fma_f32 v155, v155, s97, -v189
	v_bfe_i32 v200, v216, 17, 1
	v_add_f32_e32 v198, v198, v158
	v_and_b32_e32 v159, v200, v159
	v_exp_f32_e32 v155, v155
	v_fma_f32 v156, v156, s97, -v189
	v_add_f32_e32 v198, v198, v159
	v_bfe_i32 v199, v216, 18, 1
	v_exp_f32_e32 v156, v156
	v_and_b32_e32 v160, v199, v160
	v_fma_f32 v157, v157, s97, -v189
	v_bfe_i32 v200, v216, 19, 1
	v_add_f32_e32 v198, v198, v160
	v_and_b32_e32 v161, v200, v161
	v_exp_f32_e32 v157, v157
	v_add_f32_e32 v198, v198, v161
	v_bfe_i32 v199, v217, 0, 1
	v_fma_f32 v150, v150, s97, -v189
	v_and_b32_e32 v154, v199, v154
	v_bfe_i32 v200, v217, 1, 1
	v_add_f32_e32 v198, v198, v154
	v_and_b32_e32 v155, v200, v155
	v_exp_f32_e32 v150, v150
	v_fma_f32 v151, v151, s97, -v189
	v_add_f32_e32 v198, v198, v155
	v_bfe_i32 v199, v217, 2, 1
	v_exp_f32_e32 v151, v151
	v_and_b32_e32 v216, v199, v156
	v_fma_f32 v152, v152, s97, -v189
	v_bfe_i32 v200, v217, 3, 1
	v_add_f32_e32 v156, v198, v216
	v_and_b32_e32 v157, v200, v157
	v_exp_f32_e32 v152, v152
	v_fma_f32 v153, v153, s97, -v189
	v_add_f32_e32 v198, v156, v157
	v_bfe_i32 v156, v217, 16, 1
	v_exp_f32_e32 v153, v153
	v_and_b32_e32 v156, v156, v150
	v_bfe_i32 v199, v217, 17, 1
	v_add_f32_e32 v150, v198, v156
	v_and_b32_e32 v151, v199, v151
	v_add_f32_e32 v150, v150, v151
	v_bfe_i32 v198, v217, 18, 1
	v_sub_f32_e32 v167, v246, v189
	v_and_b32_e32 v152, v198, v152
	v_bfe_i32 v199, v217, 19, 1
	v_add_f32_e32 v150, v150, v152
	v_and_b32_e32 v153, v199, v153
	v_add_f32_e32 v198, v150, v153
	v_exp_f32_e32 v150, v167
	s_nop 0
	v_cmp_eq_f32_e32 vcc, 1.0, v150
	v_fma_f32 v215, v215, v150, v198
	s_cmp_eq_u64 vcc, exec
	s_cbranch_scc1 .LBB0_1289
	v_pk_mul_f32 v[68:69], v[68:69], v[150:151] op_sel_hi:[1,0]
	v_pk_mul_f32 v[66:67], v[66:67], v[150:151] op_sel_hi:[1,0]
	v_pk_mul_f32 v[64:65], v[64:65], v[150:151] op_sel_hi:[1,0]
	v_pk_mul_f32 v[62:63], v[62:63], v[150:151] op_sel_hi:[1,0]
	v_pk_mul_f32 v[60:61], v[60:61], v[150:151] op_sel_hi:[1,0]
	v_pk_mul_f32 v[58:59], v[58:59], v[150:151] op_sel_hi:[1,0]
	v_pk_mul_f32 v[56:57], v[56:57], v[150:151] op_sel_hi:[1,0]
	v_pk_mul_f32 v[54:55], v[54:55], v[150:151] op_sel_hi:[1,0]
	v_pk_mul_f32 v[52:53], v[52:53], v[150:151] op_sel_hi:[1,0]
	v_pk_mul_f32 v[50:51], v[50:51], v[150:151] op_sel_hi:[1,0]
	v_pk_mul_f32 v[48:49], v[48:49], v[150:151] op_sel_hi:[1,0]
	v_pk_mul_f32 v[46:47], v[46:47], v[150:151] op_sel_hi:[1,0]
	v_pk_mul_f32 v[40:41], v[40:41], v[150:151] op_sel_hi:[1,0]
	v_pk_mul_f32 v[38:39], v[38:39], v[150:151] op_sel_hi:[1,0]
	v_pk_mul_f32 v[44:45], v[44:45], v[150:151] op_sel_hi:[1,0]
	v_pk_mul_f32 v[42:43], v[42:43], v[150:151] op_sel_hi:[1,0]

.LBB0_1291:
	v_cvt_pk_bf16_f32 v162, v162, v163
	v_cvt_pk_bf16_f32 v163, v164, v165
	v_cvt_pk_bf16_f32 v164, v158, v159
	v_cvt_pk_bf16_f32 v165, v160, v161
	v_cvt_pk_bf16_f32 v158, v218, v167
	v_cvt_pk_bf16_f32 v159, v136, v135
	v_cvt_pk_bf16_f32 v160, v138, v137
	v_cvt_pk_bf16_f32 v161, v140, v139
	v_mfma_f32_16x16x32_bf16 v[54:57], v[106:109], v[162:165], v[54:57]
	v_cvt_pk_bf16_f32 v154, v154, v155
	v_cvt_pk_bf16_f32 v155, v216, v157
	v_cvt_pk_bf16_f32 v156, v156, v151
	v_mfma_f32_16x16x32_bf16 v[16:19], v[106:109], v[158:161], v[16:19]
	v_cvt_pk_bf16_f32 v157, v152, v153
	s_add_i32 s18, s18, 1
	v_mfma_f32_16x16x32_bf16 v[66:69], v[130:133], v[162:165], v[66:69]
	v_add_u32_e32 v213, 8, v213
	s_cmp_eq_u32 s17, s18
	v_mfma_f32_16x16x32_bf16 v[28:31], v[130:133], v[158:161], v[28:31]
	v_cvt_pk_bf16_f32 v130, v146, v141
	v_cvt_pk_bf16_f32 v131, v148, v147
	v_cvt_pk_bf16_f32 v132, v142, v143
	v_cvt_pk_bf16_f32 v133, v144, v145
	v_mfma_f32_16x16x32_bf16 v[54:57], v[102:105], v[154:157], v[54:57]
	s_nop 0
	v_mfma_f32_16x16x32_bf16 v[16:19], v[102:105], v[130:133], v[16:19]
	ds_read_b64_tr_b16 v[102:103], v239 offset:32768
	ds_read_b64_tr_b16 v[104:105], v239 offset:36864
	ds_read_b64_tr_b16 v[106:107], v239 offset:40960
	ds_read_b64_tr_b16 v[108:109], v239 offset:45056
	v_mfma_f32_16x16x32_bf16 v[58:61], v[118:121], v[162:165], v[58:61]
	v_mfma_f32_16x16x32_bf16 v[20:23], v[118:121], v[158:161], v[20:23]
	s_waitcnt lgkmcnt(2)
	v_mfma_f32_16x16x32_bf16 v[50:53], v[102:105], v[162:165], v[50:53]
	v_mfma_f32_16x16x32_bf16 v[12:15], v[102:105], v[158:161], v[12:15]
	v_mfma_f32_16x16x32_bf16 v[58:61], v[110:113], v[154:157], v[58:61]
	v_mfma_f32_16x16x32_bf16 v[20:23], v[110:113], v[130:133], v[20:23]
	s_waitcnt lgkmcnt(0)
	v_mfma_f32_16x16x32_bf16 v[50:53], v[106:109], v[154:157], v[50:53]
	v_mfma_f32_16x16x32_bf16 v[12:15], v[106:109], v[130:133], v[12:15]
	ds_read_b64_tr_b16 v[102:103], v240 offset:32768
	ds_read_b64_tr_b16 v[104:105], v240 offset:36864
	ds_read_b64_tr_b16 v[106:107], v240 offset:40960
	ds_read_b64_tr_b16 v[108:109], v240 offset:45056
	s_waitcnt lgkmcnt(2)
	v_mfma_f32_16x16x32_bf16 v[46:49], v[102:105], v[162:165], v[46:49]
	v_mfma_f32_16x16x32_bf16 v[8:11], v[102:105], v[158:161], v[8:11]
	s_waitcnt lgkmcnt(0)
	v_mfma_f32_16x16x32_bf16 v[46:49], v[106:109], v[154:157], v[46:49]
	v_mfma_f32_16x16x32_bf16 v[8:11], v[106:109], v[130:133], v[8:11]
	ds_read_b64_tr_b16 v[102:103], v241 offset:32768
	ds_read_b64_tr_b16 v[104:105], v241 offset:36864
	ds_read_b64_tr_b16 v[106:107], v241 offset:40960
	ds_read_b64_tr_b16 v[108:109], v241 offset:45056
	s_waitcnt lgkmcnt(2)
	v_mfma_f32_16x16x32_bf16 v[38:41], v[102:105], v[162:165], v[38:41]
	v_mfma_f32_16x16x32_bf16 v[4:7], v[102:105], v[158:161], v[4:7]
	ds_read_b64_tr_b16 v[110:111], v242 offset:32768
	ds_read_b64_tr_b16 v[112:113], v242 offset:36864
	s_waitcnt lgkmcnt(2)
	v_mfma_f32_16x16x32_bf16 v[38:41], v[106:109], v[154:157], v[38:41]
	v_mfma_f32_16x16x32_bf16 v[4:7], v[106:109], v[130:133], v[4:7]
	ds_read_b64_tr_b16 v[104:105], v242 offset:40960
	ds_read_b64_tr_b16 v[106:107], v242 offset:45056
	s_waitcnt vmcnt(0)
	v_mfma_f32_16x16x32_bf16 v[62:65], v[126:129], v[162:165], v[62:65]
	s_waitcnt lgkmcnt(0)
	s_barrier
	v_mfma_f32_16x16x32_bf16 v[24:27], v[126:129], v[158:161], v[24:27]
	v_mfma_f32_16x16x32_bf16 v[42:45], v[110:113], v[162:165], v[42:45]
	v_mfma_f32_16x16x32_bf16 v[0:3], v[110:113], v[158:161], v[0:3]
	v_mfma_f32_16x16x32_bf16 v[66:69], v[122:125], v[154:157], v[66:69]
	v_mfma_f32_16x16x32_bf16 v[28:31], v[122:125], v[130:133], v[28:31]
	v_mfma_f32_16x16x32_bf16 v[62:65], v[114:117], v[154:157], v[62:65]
	v_mfma_f32_16x16x32_bf16 v[24:27], v[114:117], v[130:133], v[24:27]
	v_mfma_f32_16x16x32_bf16 v[42:45], v[104:107], v[154:157], v[42:45]
	v_mfma_f32_16x16x32_bf16 v[0:3], v[104:107], v[130:133], v[0:3]
	s_cbranch_scc0 .Lat16_O_1283
	v_mov_b32_e32 v167, v215
	v_mov_b32_e32 v198, v245
	s_nop 1
	v_permlane16_swap_b32_e32 v215, v167
	v_permlane16_swap_b32_e32 v245, v198
	v_add_f32_e32 v167, v215, v167
	v_add_f32_e32 v198, v245, v198
	v_mov_b32_e32 v217, v167
	v_mov_b32_e32 v248, v198
	s_nop 1
	v_permlane32_swap_b32_e32 v167, v217
	v_permlane32_swap_b32_e32 v198, v248
	v_add_f32_e32 v103, v167, v217
	v_add_f32_e32 v102, v198, v248
	s_branch .LBB0_1280

.Lat16_O_1285:
	s_andn2_b64 vcc, exec, s[8:9]
	s_cbranch_vccnz .Lat16_O_1287
	s_mov_b32 s20, s11
	s_mov_b32 m0, s20
	s_nop 0
	global_load_lds_dwordx4 v32, s[100:101]
	s_add_i32 m0, s20, 0x8000
	s_nop 0
	global_load_lds_dwordx4 v166, s[100:101]
	s_add_i32 m0, s20, 0x400
	s_nop 0
	global_load_lds_dwordx4 v186, s[100:101]
	s_add_i32 m0, s20, 0x8400
	s_nop 0
	global_load_lds_dwordx4 v188, s[100:101]
	s_add_u32 s100, s100, 0x240000
	s_addc_u32 s101, s101, 0
.Lat16_O_1287:
	ds_read_b128 v[102:105], v171 offset:16384
	ds_read_b128 v[106:109], v219 offset:16384
	ds_read_b128 v[110:113], v222 offset:16384
	ds_read_b128 v[114:117], v223 offset:16384
	ds_read_b128 v[118:121], v171 offset:20480
	ds_read_b128 v[122:125], v219 offset:20480
	ds_read_b128 v[126:129], v222 offset:20480
	ds_read_b128 v[130:133], v223 offset:20480
	s_waitcnt lgkmcnt(0)
	v_mfma_f32_16x16x32_bf16 v[138:141], v[118:121], v[78:81], 0
	v_mfma_f32_16x16x32_bf16 v[134:137], v[102:105], v[78:81], 0
	v_mfma_f32_16x16x32_bf16 v[102:105], v[102:105], v[94:97], 0
	v_mfma_f32_16x16x32_bf16 v[118:121], v[118:121], v[94:97], 0
	v_mfma_f32_16x16x32_bf16 v[134:137], v[106:109], v[70:73], v[134:137]
	v_mfma_f32_16x16x32_bf16 v[102:105], v[106:109], v[86:89], v[102:105]
	v_mfma_f32_16x16x32_bf16 v[138:141], v[122:125], v[70:73], v[138:141]
	v_mfma_f32_16x16x32_bf16 v[118:121], v[122:125], v[86:89], v[118:121]
	v_mfma_f32_16x16x32_bf16 v[134:137], v[110:113], v[74:77], v[134:137]
	v_mfma_f32_16x16x32_bf16 v[102:105], v[110:113], v[90:93], v[102:105]
	v_mfma_f32_16x16x32_bf16 v[138:141], v[126:129], v[74:77], v[138:141]
	v_mfma_f32_16x16x32_bf16 v[118:121], v[126:129], v[90:93], v[118:121]
	v_mfma_f32_16x16x32_bf16 v[162:165], v[114:117], v[82:85], v[134:137]
	v_mfma_f32_16x16x32_bf16 v[134:137], v[114:117], v[98:101], v[102:105]
	s_nop 3
	ds_read_b128 v[102:105], v171 offset:24576
	ds_read_b128 v[106:109], v219 offset:24576
	ds_read_b128 v[110:113], v222 offset:24576
	ds_read_b128 v[114:117], v223 offset:24576
	v_max_f32_e32 v167, v164, v165
	v_mfma_f32_16x16x32_bf16 v[158:161], v[130:133], v[82:85], v[138:141]
	v_max3_f32 v167, v162, v163, v167
	v_mfma_f32_16x16x32_bf16 v[138:141], v[130:133], v[98:101], v[118:121]
	s_nop 2
	ds_read_b128 v[118:121], v171 offset:28672
	ds_read_b128 v[122:125], v219 offset:28672
	ds_read_b128 v[126:129], v222 offset:28672
	ds_read_b128 v[130:133], v223 offset:28672
	v_max3_f32 v189, v159, v160, v161
	v_max3_f32 v167, v167, v158, v189
	s_waitcnt lgkmcnt(0)
	v_mfma_f32_16x16x32_bf16 v[142:145], v[102:105], v[78:81], 0
	v_mfma_f32_16x16x32_bf16 v[102:105], v[102:105], v[94:97], 0
	v_mfma_f32_16x16x32_bf16 v[102:105], v[106:109], v[86:89], v[102:105]
	v_mfma_f32_16x16x32_bf16 v[102:105], v[110:113], v[90:93], v[102:105]
	v_mfma_f32_16x16x32_bf16 v[146:149], v[114:117], v[98:101], v[102:105]
	v_mfma_f32_16x16x32_bf16 v[102:105], v[118:121], v[78:81], 0
	v_mfma_f32_16x16x32_bf16 v[142:145], v[106:109], v[70:73], v[142:145]
	v_mfma_f32_16x16x32_bf16 v[102:105], v[122:125], v[70:73], v[102:105]
	v_mfma_f32_16x16x32_bf16 v[142:145], v[110:113], v[74:77], v[142:145]
	v_mfma_f32_16x16x32_bf16 v[102:105], v[126:129], v[74:77], v[102:105]
	v_mfma_f32_16x16x32_bf16 v[154:157], v[114:117], v[82:85], v[142:145]
	v_mfma_f32_16x16x32_bf16 v[150:153], v[130:133], v[82:85], v[102:105]
	v_mfma_f32_16x16x32_bf16 v[102:105], v[118:121], v[94:97], 0
	s_nop 5
	v_max3_f32 v189, v155, v156, v157
	v_max3_f32 v167, v167, v154, v189
	v_max3_f32 v189, v151, v152, v153
	v_mfma_f32_16x16x32_bf16 v[102:105], v[122:125], v[86:89], v[102:105]
	v_max3_f32 v167, v167, v150, v189
	v_mov_b32_e32 v189, v167
	s_nop 1
	v_permlane16_swap_b32_e32 v167, v189
	v_mfma_f32_16x16x32_bf16 v[102:105], v[126:129], v[90:93], v[102:105]
	v_max_f32 v167, v167, v189
	s_nop 0
	v_mov_b32_e32 v189, v167
	s_nop 1
	v_permlane32_swap_b32_e32 v167, v189
	v_max_f32 v167, v167, v189
	v_mfma_f32_16x16x32_bf16 v[142:145], v[130:133], v[98:101], v[102:105]
	v_mul_f32_e32 v167, 0x3e0293ee, v167
	v_add_f32_e32 v189, 0x41000000, v246
	v_cmp_gt_f32_e32 vcc, v167, v189
	ds_read_b64_tr_b16 v[130:131], v224 offset:49152
	ds_read_b64_tr_b16 v[132:133], v224 offset:53248
	ds_read_b64_tr_b16 v[122:123], v224 offset:57344
	ds_read_b64_tr_b16 v[124:125], v224 offset:61440
	ds_read_b64_tr_b16 v[126:127], v225 offset:49152
	ds_read_b64_tr_b16 v[128:129], v225 offset:53248
	ds_read_b64_tr_b16 v[114:115], v225 offset:57344
	ds_read_b64_tr_b16 v[116:117], v225 offset:61440
	v_cndmask_b32_e32 v189, v246, v167, vcc
	ds_read_b64_tr_b16 v[118:119], v237 offset:49152
	ds_read_b64_tr_b16 v[120:121], v237 offset:53248
	ds_read_b64_tr_b16 v[110:111], v237 offset:57344
	ds_read_b64_tr_b16 v[112:113], v237 offset:61440
	ds_read_b64_tr_b16 v[106:107], v238 offset:49152
	ds_read_b64_tr_b16 v[108:109], v238 offset:53248
	ds_read_b64_tr_b16 v[102:103], v238 offset:57344
	ds_read_b64_tr_b16 v[104:105], v238 offset:61440
	ds_read_b64 v[198:199], v213
	v_fma_f32 v162, v162, s97, -v189
	v_exp_f32_e32 v162, v162
	v_fma_f32 v163, v163, s97, -v189
	v_exp_f32_e32 v163, v163
	v_fma_f32 v164, v164, s97, -v189
	v_exp_f32_e32 v164, v164
	v_fma_f32 v165, v165, s97, -v189
	v_exp_f32_e32 v165, v165
	v_fma_f32 v158, v158, s97, -v189
	s_waitcnt lgkmcnt(0)
	v_lshrrev_b64 v[216:217], v170, v[198:199]
	v_bfe_i32 v198, v216, 0, 1
	v_exp_f32_e32 v158, v158
	v_and_b32_e32 v162, v198, v162
	v_fma_f32 v159, v159, s97, -v189
	v_bfe_i32 v199, v216, 1, 1
	v_and_b32_e32 v163, v199, v163
	v_exp_f32_e32 v159, v159
	v_fma_f32 v160, v160, s97, -v189
	v_add_f32_e32 v198, v162, v163
	v_bfe_i32 v199, v216, 2, 1
	v_exp_f32_e32 v160, v160
	v_and_b32_e32 v164, v199, v164
	v_fma_f32 v161, v161, s97, -v189
	v_bfe_i32 v200, v216, 3, 1
	v_add_f32_e32 v198, v198, v164
	v_and_b32_e32 v165, v200, v165
	v_exp_f32_e32 v161, v161
	v_fma_f32 v154, v154, s97, -v189
	v_add_f32_e32 v198, v198, v165
	v_bfe_i32 v199, v216, 16, 1
	v_exp_f32_e32 v154, v154
	v_and_b32_e32 v158, v199, v158
	v_fma_f32 v155, v155, s97, -v189
	v_bfe_i32 v200, v216, 17, 1
	v_add_f32_e32 v198, v198, v158
	v_and_b32_e32 v159, v200, v159
	v_exp_f32_e32 v155, v155
	v_fma_f32 v156, v156, s97, -v189
	v_add_f32_e32 v198, v198, v159
	v_bfe_i32 v199, v216, 18, 1
	v_exp_f32_e32 v156, v156
	v_and_b32_e32 v160, v199, v160
	v_fma_f32 v157, v157, s97, -v189
	v_bfe_i32 v200, v216, 19, 1
	v_add_f32_e32 v198, v198, v160
	v_and_b32_e32 v161, v200, v161
	v_exp_f32_e32 v157, v157
	v_add_f32_e32 v198, v198, v161
	v_bfe_i32 v199, v217, 0, 1
	v_fma_f32 v150, v150, s97, -v189
	v_and_b32_e32 v154, v199, v154
	v_bfe_i32 v200, v217, 1, 1
	v_add_f32_e32 v198, v198, v154
	v_and_b32_e32 v155, v200, v155
	v_exp_f32_e32 v150, v150
	v_fma_f32 v151, v151, s97, -v189
	v_add_f32_e32 v198, v198, v155
	v_bfe_i32 v199, v217, 2, 1
	v_exp_f32_e32 v151, v151
	v_and_b32_e32 v216, v199, v156
	v_fma_f32 v152, v152, s97, -v189
	v_bfe_i32 v200, v217, 3, 1
	v_add_f32_e32 v156, v198, v216
	v_and_b32_e32 v157, v200, v157
	v_exp_f32_e32 v152, v152
	v_fma_f32 v153, v153, s97, -v189
	v_add_f32_e32 v198, v156, v157
	v_bfe_i32 v156, v217, 16, 1
	v_exp_f32_e32 v153, v153
	v_and_b32_e32 v156, v156, v150
	v_bfe_i32 v199, v217, 17, 1
	v_add_f32_e32 v150, v198, v156
	v_and_b32_e32 v151, v199, v151
	v_add_f32_e32 v150, v150, v151
	v_bfe_i32 v198, v217, 18, 1
	v_sub_f32_e32 v167, v246, v189
	v_and_b32_e32 v152, v198, v152
	v_bfe_i32 v199, v217, 19, 1
	v_add_f32_e32 v150, v150, v152
	v_and_b32_e32 v153, v199, v153
	v_add_f32_e32 v198, v150, v153
	v_exp_f32_e32 v150, v167
	s_nop 0
	v_cmp_eq_f32_e32 vcc, 1.0, v150
	v_fma_f32 v215, v215, v150, v198
	s_cmp_eq_u64 vcc, exec
	s_cbranch_scc1 .Lat16_O_1289
	v_pk_mul_f32 v[68:69], v[68:69], v[150:151] op_sel_hi:[1,0]
	v_pk_mul_f32 v[66:67], v[66:67], v[150:151] op_sel_hi:[1,0]
	v_pk_mul_f32 v[64:65], v[64:65], v[150:151] op_sel_hi:[1,0]
	v_pk_mul_f32 v[62:63], v[62:63], v[150:151] op_sel_hi:[1,0]
	v_pk_mul_f32 v[60:61], v[60:61], v[150:151] op_sel_hi:[1,0]
	v_pk_mul_f32 v[58:59], v[58:59], v[150:151] op_sel_hi:[1,0]
	v_pk_mul_f32 v[56:57], v[56:57], v[150:151] op_sel_hi:[1,0]
	v_pk_mul_f32 v[54:55], v[54:55], v[150:151] op_sel_hi:[1,0]
	v_pk_mul_f32 v[52:53], v[52:53], v[150:151] op_sel_hi:[1,0]
	v_pk_mul_f32 v[50:51], v[50:51], v[150:151] op_sel_hi:[1,0]
	v_pk_mul_f32 v[48:49], v[48:49], v[150:151] op_sel_hi:[1,0]
	v_pk_mul_f32 v[46:47], v[46:47], v[150:151] op_sel_hi:[1,0]
	v_pk_mul_f32 v[40:41], v[40:41], v[150:151] op_sel_hi:[1,0]
	v_pk_mul_f32 v[38:39], v[38:39], v[150:151] op_sel_hi:[1,0]
	v_pk_mul_f32 v[44:45], v[44:45], v[150:151] op_sel_hi:[1,0]
	v_pk_mul_f32 v[42:43], v[42:43], v[150:151] op_sel_hi:[1,0]

.Lat16_O_1291:
	v_cvt_pk_bf16_f32 v162, v162, v163
	v_cvt_pk_bf16_f32 v163, v164, v165
	v_cvt_pk_bf16_f32 v164, v158, v159
	v_cvt_pk_bf16_f32 v165, v160, v161
	v_cvt_pk_bf16_f32 v158, v218, v167
	v_cvt_pk_bf16_f32 v159, v136, v135
	v_cvt_pk_bf16_f32 v160, v138, v137
	v_cvt_pk_bf16_f32 v161, v140, v139
	v_mfma_f32_16x16x32_bf16 v[54:57], v[106:109], v[162:165], v[54:57]
	v_cvt_pk_bf16_f32 v154, v154, v155
	v_cvt_pk_bf16_f32 v155, v216, v157
	v_cvt_pk_bf16_f32 v156, v156, v151
	v_mfma_f32_16x16x32_bf16 v[16:19], v[106:109], v[158:161], v[16:19]
	v_cvt_pk_bf16_f32 v157, v152, v153
	s_add_i32 s18, s18, 1
	v_mfma_f32_16x16x32_bf16 v[66:69], v[130:133], v[162:165], v[66:69]
	v_add_u32_e32 v213, 8, v213
	s_cmp_eq_u32 s17, s18
	v_mfma_f32_16x16x32_bf16 v[28:31], v[130:133], v[158:161], v[28:31]
	v_cvt_pk_bf16_f32 v130, v146, v141
	v_cvt_pk_bf16_f32 v131, v148, v147
	v_cvt_pk_bf16_f32 v132, v142, v143
	v_cvt_pk_bf16_f32 v133, v144, v145
	v_mfma_f32_16x16x32_bf16 v[54:57], v[102:105], v[154:157], v[54:57]
	s_nop 0
	v_mfma_f32_16x16x32_bf16 v[16:19], v[102:105], v[130:133], v[16:19]
	ds_read_b64_tr_b16 v[102:103], v239 offset:49152
	ds_read_b64_tr_b16 v[104:105], v239 offset:53248
	ds_read_b64_tr_b16 v[106:107], v239 offset:57344
	ds_read_b64_tr_b16 v[108:109], v239 offset:61440
	v_mfma_f32_16x16x32_bf16 v[58:61], v[118:121], v[162:165], v[58:61]
	v_mfma_f32_16x16x32_bf16 v[20:23], v[118:121], v[158:161], v[20:23]
	s_waitcnt lgkmcnt(2)
	v_mfma_f32_16x16x32_bf16 v[50:53], v[102:105], v[162:165], v[50:53]
	v_mfma_f32_16x16x32_bf16 v[12:15], v[102:105], v[158:161], v[12:15]
	v_mfma_f32_16x16x32_bf16 v[58:61], v[110:113], v[154:157], v[58:61]
	v_mfma_f32_16x16x32_bf16 v[20:23], v[110:113], v[130:133], v[20:23]
	s_waitcnt lgkmcnt(0)
	v_mfma_f32_16x16x32_bf16 v[50:53], v[106:109], v[154:157], v[50:53]
	v_mfma_f32_16x16x32_bf16 v[12:15], v[106:109], v[130:133], v[12:15]
	ds_read_b64_tr_b16 v[102:103], v240 offset:49152
	ds_read_b64_tr_b16 v[104:105], v240 offset:53248
	ds_read_b64_tr_b16 v[106:107], v240 offset:57344
	ds_read_b64_tr_b16 v[108:109], v240 offset:61440
	s_waitcnt lgkmcnt(2)
	v_mfma_f32_16x16x32_bf16 v[46:49], v[102:105], v[162:165], v[46:49]
	v_mfma_f32_16x16x32_bf16 v[8:11], v[102:105], v[158:161], v[8:11]
	s_waitcnt lgkmcnt(0)
	v_mfma_f32_16x16x32_bf16 v[46:49], v[106:109], v[154:157], v[46:49]
	v_mfma_f32_16x16x32_bf16 v[8:11], v[106:109], v[130:133], v[8:11]
	ds_read_b64_tr_b16 v[102:103], v241 offset:49152
	ds_read_b64_tr_b16 v[104:105], v241 offset:53248
	ds_read_b64_tr_b16 v[106:107], v241 offset:57344
	ds_read_b64_tr_b16 v[108:109], v241 offset:61440
	s_waitcnt lgkmcnt(2)
	v_mfma_f32_16x16x32_bf16 v[38:41], v[102:105], v[162:165], v[38:41]
	v_mfma_f32_16x16x32_bf16 v[4:7], v[102:105], v[158:161], v[4:7]
	ds_read_b64_tr_b16 v[110:111], v242 offset:49152
	ds_read_b64_tr_b16 v[112:113], v242 offset:53248
	s_waitcnt lgkmcnt(2)
	v_mfma_f32_16x16x32_bf16 v[38:41], v[106:109], v[154:157], v[38:41]
	v_mfma_f32_16x16x32_bf16 v[4:7], v[106:109], v[130:133], v[4:7]
	ds_read_b64_tr_b16 v[104:105], v242 offset:57344
	ds_read_b64_tr_b16 v[106:107], v242 offset:61440
	s_waitcnt vmcnt(0)
	v_mfma_f32_16x16x32_bf16 v[62:65], v[126:129], v[162:165], v[62:65]
	s_waitcnt lgkmcnt(0)
	s_barrier
	v_mfma_f32_16x16x32_bf16 v[24:27], v[126:129], v[158:161], v[24:27]
	v_mfma_f32_16x16x32_bf16 v[42:45], v[110:113], v[162:165], v[42:45]
	v_mfma_f32_16x16x32_bf16 v[0:3], v[110:113], v[158:161], v[0:3]
	v_mfma_f32_16x16x32_bf16 v[66:69], v[122:125], v[154:157], v[66:69]
	v_mfma_f32_16x16x32_bf16 v[28:31], v[122:125], v[130:133], v[28:31]
	v_mfma_f32_16x16x32_bf16 v[62:65], v[114:117], v[154:157], v[62:65]
	v_mfma_f32_16x16x32_bf16 v[24:27], v[114:117], v[130:133], v[24:27]
	v_mfma_f32_16x16x32_bf16 v[42:45], v[104:107], v[154:157], v[42:45]
	v_mfma_f32_16x16x32_bf16 v[0:3], v[104:107], v[130:133], v[0:3]
	s_cbranch_scc0 .LBB0_1283
	v_mov_b32_e32 v167, v215
	v_mov_b32_e32 v198, v245
	s_nop 1
	v_permlane16_swap_b32_e32 v215, v167
	v_permlane16_swap_b32_e32 v245, v198
	v_add_f32_e32 v167, v215, v167
	v_add_f32_e32 v198, v245, v198
	v_mov_b32_e32 v217, v167
	v_mov_b32_e32 v248, v198
	s_nop 1
	v_permlane32_swap_b32_e32 v167, v217
	v_permlane32_swap_b32_e32 v198, v248
	v_add_f32_e32 v103, v167, v217
	v_add_f32_e32 v102, v198, v248
	s_branch .LBB0_1280
